# indexer-score and attention tasks mapped by XCD-contiguous workgroup index (one batch x kv-group per XCD in the attention phase) on top of the previous version
# baseline (speedup 1.0000x reference)
; #define LAS __attribute__((address_space(3)))
; __device__ __forceinline__ void xcd_barrier_complete(unsigned* bar, unsigned x, unsigned& nloc, unsigned& nx) {
;     const unsigned G = gridDim.x * gridDim.y * gridDim.z;
;     unsigned sum, cnt, mine, sp = 0u;
;     for (;;) {
;         sum = 0u; cnt = 0u; mine = 0u;
; #pragma unroll
;         for (unsigned j = 0; j < 16; ++j) { const unsigned c = xb_ld(&bar[XB_XCNT(j)]); sum += c; cnt += (c > 0u) ? 1u : 0u; mine = (j == x) ? c : mine; }
;         if (sum == G) break;
;         __builtin_amdgcn_s_sleep(1);
;         if ((++sp & 255u) == 0u) { if (xb_ld(&bar[XB_TMO])) break; if (sp > XB_SPIN_CAP) { atomicAdd(&bar[XB_TMO], 1u); break; } }
;     }
;     nloc = mine > 0u ? mine : 1u; nx = cnt > 0u ? cnt : 1u;
; }
; __global__ void __launch_bounds__(NTHR, 2) mk_fwd(Args args) {
;     ...
;     unsigned char* ws = args.ws;
;     F.ctl = (unsigned*)(ws + WS_CTL);
;     F.x_in = args.in[0]; F.gains = args.in[1]; F.w_in = args.in[2]; F.pool_w = args.in[3]; F.pool_scale = args.in[4]; F.conv_w = args.in[5]; F.rel_bias = args.in[6];
;     F.w_branch = args.in[7]; F.w_gate = args.in[8]; F.b_gate = args.in[9]; F.w_out = args.in[10]; F.w_up = args.in[11]; F.w_down = args.in[12]; F.out = args.out;
;     F.Wcat1 = (bf16*)(ws + WS_WCAT1); F.W8g = ws + WS_W8G; F.H8 = ws + WS_H8; F.Wpool = (bf16*)(ws + WS_WPOOL); F.Wbr = (bf16*)(ws + WS_WBR); F.Wbrx = (bf16*)(ws + WS_WBRX); F.Wout = (bf16*)(ws + WS_WOUT); F.Wup = (bf16*)(ws + WS_WUP); F.Wdown = (bf16*)(ws + WS_WDOWN);
;     F.Hb = (bf16*)(ws + WS_H); F.PROJ = (bf16*)(ws + WS_PROJ); F.GATES = (bf16*)(ws + WS_GATES); F.ABUF = (bf16*)(ws + WS_ABUF); F.Y = (bf16*)(ws + WS_Y); F.MP = (bf16*)(ws + WS_MP);
;     F.SC = (float*)(ws + WS_SC); F.MASK = (unsigned long long*)(ws + WS_MASK);
;     for (int u = (int)threadIdx.x; u < (LDS_BYTES - LDSCTL_OFF) / 4; u += NTHR) ((LAS unsigned*)(F.lds + LDSCTL_OFF))[u] = 0u;
;     __syncthreads();
;     for (int idx = (int)threadIdx.x; idx < 8 * 129; idx += NTHR) { const int hd = idx / 129, d = idx - hd * 129; ((LAS float*)(F.lds + LUT_OFF))[hd * 132 + d] = F.rel_bias[t5_bucket(d) * NH + hd] * 1.4426950408889634f; }
;     __syncthreads();
;     XcdBarrier bar; bar.bar = F.ctl + CW_BAR; bar.x = 0; bar.st = nullptr;
;     if (!MK_SPLIT) bar = xcd_barrier_post(F.ctl + CW_BAR, F.MISC + 8);
.LBB0_95:
	s_add_u32 s0, s26, 0x17500000
	s_addc_u32 s1, s27, 0
	v_writelane_b32 v251, s0, 34
	s_mul_i32 s28, s35, 0x36000
	s_mov_b32 s63, 0
	v_writelane_b32 v251, s1, 35
	s_add_u32 s0, s26, 0x4100000
	s_addc_u32 s1, s27, 0
	s_add_u32 s96, s26, 0xa900000
	s_addc_u32 s97, s27, 0
	s_add_u32 s39, s26, 0x1f500000
	v_writelane_b32 v251, s0, 36
	s_addc_u32 s24, s27, 0
	v_mov_b32_e32 v193, 0
	v_writelane_b32 v251, s1, 37
	s_add_u32 s0, s26, 0x6900000
	s_addc_u32 s1, s27, 0
	v_writelane_b32 v251, s0, 38
	v_mov_b32_e32 v245, 0x80
	v_mov_b32_e32 v246, 0x7fc07fc0
	v_writelane_b32 v251, s1, 39
	s_add_u32 s0, s26, 0x18500000
	s_addc_u32 s1, s27, 0
	v_writelane_b32 v251, s0, 40
	s_movk_i32 s94, 0x3600
	s_movk_i32 s95, 0x2000
	v_writelane_b32 v251, s1, 41
	s_add_u32 s0, s26, 0x4900000
	s_addc_u32 s1, s27, 0
	v_writelane_b32 v251, s0, 42
	s_mov_b32 s70, 0x14000
	s_mov_b32 s71, 0x18000
	v_writelane_b32 v251, s1, 43
	s_add_u32 s0, s26, 0x8900000
	s_addc_u32 s1, s27, 0
	v_writelane_b32 v251, s0, 44
	s_mov_b32 s33, 0x1c000
	s_mov_b32 s92, 0xffff0000
	v_writelane_b32 v251, s1, 45
	s_add_u32 s0, s26, 0x11500000
	v_writelane_b32 v251, s0, 46
	s_addc_u32 s0, s27, 0
	s_add_u32 s76, s26, 0x23700000
	s_addc_u32 s77, s27, 0
	s_cmpk_lt_i32 s31, 0x300
	v_writelane_b32 v251, s0, 47
	s_cselect_b64 s[0:1], -1, 0
	v_writelane_b32 v251, s0, 48
	s_ashr_i32 s15, s31, 31
	s_ashr_i32 s25, s34, 31
	v_writelane_b32 v251, s1, 49
	s_lshr_b32 s0, s15, 29
	s_add_i32 s0, s31, s0
	s_ashr_i32 s7, s0, 3
	s_and_b32 s0, s0, -8
	s_sub_i32 s11, s31, s0
	s_cmpk_gt_i32 s31, 0x9f
	s_cselect_b64 s[0:1], -1, 0
	v_writelane_b32 v251, s0, 50
	s_mov_b32 s74, 0x40000
	s_mov_b32 s75, 0x48000
	v_writelane_b32 v251, s1, 51
	s_add_u32 s0, s26, 0x2800000
	s_addc_u32 s1, s27, 0
	v_writelane_b32 v251, s0, 52
	s_add_i32 s10, s34, 0xffffff60
	s_add_i32 s12, s31, 0xffffff60
	v_writelane_b32 v251, s1, 53
	s_add_u32 s0, s26, 0xa902000
	s_addc_u32 s1, s27, 0
	v_writelane_b32 v251, s0, 54
	s_cmpk_lt_u32 s12, 0xc0
	s_mov_b32 s67, 0x50000
	v_writelane_b32 v251, s1, 55
	s_cselect_b64 s[0:1], -1, 0
	v_writelane_b32 v251, s0, 56
	s_mov_b32 s66, 0x20000
	s_mov_b32 s68, 0x30000
	v_writelane_b32 v251, s1, 57
	s_and_b32 s0, s31, 7
	s_lshr_b32 s1, s12, 3
	s_mul_i32 s0, s0, 24
	s_add_i32 s0, s0, s1
	s_and_b32 s2, s0, 0xff
	s_mulk_i32 s2, 0xab
	s_lshr_b32 s6, s2, 13
	s_lshl_b32 s2, s6, 3
	s_and_b32 s3, s2, 56
	s_sub_i32 s3, 32, s3
	s_mul_i32 s6, s6, 48
	s_min_u32 s3, s3, 8
	s_sub_i32 s6, s0, s6
	s_ashr_i32 s0, s10, 31
	v_writelane_b32 v251, s10, 58
	s_cmpk_lt_i32 s31, 0x2a0
	v_writelane_b32 v251, s0, 59
	s_cselect_b64 s[16:17], -1, 0
	v_writelane_b32 v251, s16, 60
	s_cmp_lt_u32 s12, 32
	v_cvt_f32_ubyte0_e32 v0, s3
	v_writelane_b32 v251, s17, 61
	v_writelane_b32 v251, s12, 62
	s_cselect_b64 s[12:13], -1, 0
	s_lshl_b32 s0, s31, 2
	s_and_b32 s0, s0, 4
	v_writelane_b32 v251, s12, 63
	s_or_b32 s0, s0, s1
	s_bfe_u32 s1, s31, 0x20001
	v_writelane_b32 v252, s13, 0
	v_writelane_b32 v252, s0, 1
	s_lshl_b32 s10, s1, 17
	v_writelane_b32 v252, s10, 2
	v_writelane_b32 v252, s1, 3
	s_lshl_b32 s1, s1, 9
	v_writelane_b32 v252, s1, 4
	s_lshl_b32 s1, s35, 14
	s_lshl_b32 s10, s31, 1
	s_lshl_b32 s0, s0, 18
	s_add_i32 s1, s1, 0
	s_addk_i32 s10, 0xa0
	s_add_u32 s12, s26, 0x4200
	v_writelane_b32 v252, s1, 5
	s_addc_u32 s13, s27, 0
	v_writelane_b32 v252, s12, 6
	v_readlane_b32 s20, v251, 2
	v_readlane_b32 s22, v251, 4
	v_writelane_b32 v252, s13, 7
	s_add_u32 s12, s26, 0x4400
	s_addc_u32 s13, s27, 0
	v_writelane_b32 v252, s12, 8
	v_readlane_b32 s23, v251, 5
	v_readlane_b32 s21, v251, 3
	v_writelane_b32 v252, s13, 9
	s_add_u32 s12, s26, 0x4500
	s_addc_u32 s13, s27, 0
	v_writelane_b32 v252, s12, 10
	v_rcp_iflag_f32_e32 v1, v0
	v_cvt_f32_ubyte0_e32 v2, s6
	v_writelane_b32 v252, s13, 11
	s_add_u32 s12, s26, 0x4600
	s_addc_u32 s13, s27, 0
	v_writelane_b32 v252, s12, 12
	v_mul_f32_e32 v1, v2, v1
	v_trunc_f32_e32 v1, v1
	v_writelane_b32 v252, s13, 13
	s_add_u32 s12, s26, 0x4700
	s_addc_u32 s13, s27, 0
	v_writelane_b32 v252, s12, 14
	v_fma_f32 v2, -v1, v0, v2
	s_mov_b32 s69, 0x60000
	v_writelane_b32 v252, s13, 15
	s_add_u32 s12, s26, 0x4800
	s_addc_u32 s13, s27, 0
	v_writelane_b32 v252, s12, 16
	s_mov_b32 s64, 0x70000
	s_mov_b32 s65, 0x40c00000
	v_writelane_b32 v252, s13, 17
	s_add_u32 s12, s26, 0x4900
	s_addc_u32 s13, s27, 0
	v_writelane_b32 v252, s12, 18
	s_mov_b64 s[52:53], 0x2000
	s_nop 0
	v_writelane_b32 v252, s13, 19
	s_add_u32 s12, s26, 0x4a00
	s_addc_u32 s13, s27, 0
	v_writelane_b32 v252, s12, 20
	s_nop 1
	v_writelane_b32 v252, s13, 21
	s_add_u32 s12, s26, 0x4b00
	s_addc_u32 s13, s27, 0
	v_writelane_b32 v252, s12, 22
	s_nop 1
	v_writelane_b32 v252, s13, 23
	s_add_u32 s12, s26, 0x4c00
	s_addc_u32 s13, s27, 0
	v_writelane_b32 v252, s12, 24
	s_nop 1
	v_writelane_b32 v252, s13, 25
	s_add_u32 s12, s26, 0x4d00
	s_addc_u32 s13, s27, 0
	v_writelane_b32 v252, s12, 26
	s_nop 1
	v_writelane_b32 v252, s13, 27
	s_add_u32 s12, s26, 0x4e00
	s_addc_u32 s13, s27, 0
	v_writelane_b32 v252, s12, 28
	s_nop 1
	v_writelane_b32 v252, s13, 29
	s_add_u32 s12, s26, 0x4f00
	s_addc_u32 s13, s27, 0
	v_writelane_b32 v252, s12, 30
	s_nop 1
	v_writelane_b32 v252, s13, 31
	s_add_u32 s12, s26, 0x5000
	s_addc_u32 s13, s27, 0
	v_writelane_b32 v252, s12, 32
	s_nop 1
	v_writelane_b32 v252, s13, 33
	s_add_u32 s12, s26, 0x5100
	s_addc_u32 s13, s27, 0
	v_writelane_b32 v252, s12, 34
	s_nop 1
	v_writelane_b32 v252, s13, 35
	s_add_u32 s12, s26, 0x5200
	s_addc_u32 s13, s27, 0
	v_writelane_b32 v252, s12, 36
	s_nop 1
	v_writelane_b32 v252, s13, 37
	s_add_u32 s12, s26, 0x5300
	s_addc_u32 s13, s27, 0
	v_writelane_b32 v252, s12, 38
	s_cmp_eq_u32 s9, 15
	s_nop 0
	v_writelane_b32 v252, s13, 39
; #define LAS __attribute__((address_space(3)))
; __device__ __forceinline__ int lane_id() { int l; asm volatile("s_nop 4\n\tv_mbcnt_lo_u32_b32 %0, -1, 0\n\tv_mbcnt_hi_u32_b32 %0, -1, %0\n\ts_nop 4" : "=v"(l)); return l; }
; __device__ __forceinline__ void scores_phase_mfma(Frame& F) {
;     ...
;         const int lane = lane_id(), c = lane & 15, q4 = lane >> 4;
;         const int j = blockIdx.x, b = j >> 6, i = j & 63, tb = rep == 0 ? 127 - i : i, t0 = tb * 16, nt = tb + 1;
;         const bf16* qrow = F.PROJ + (size_t)(b * SEQ + t0 + c) * INWP + O_QI + 8 * q4;
; __device__ __forceinline__ void attn_phase_mfma(Frame& F) {
;     ...
;     const int lane = tid & 63, wave = F.wave, grp = wave >> 2, hr = wave & 3, c = lane & 31, hh = lane >> 5, tg = tid & 255;
;     LAS unsigned char* KB0 = F.lds + RING_OFF + AT_KBUF + grp * (2 * 32 * AT_KPITCH);
;     LAS unsigned char* VB0 = F.lds + RING_OFF + AT_VBUF + grp * (2 * 128 * AT_VPITCH);
;     const LAS float* LUT = (const LAS float*)(F.lds + LUT_OFF);
;     LAS float* MG = (LAS float*)(F.lds + RING_OFF + AT_MERGE) + hr * (66 * 64);
;     const float C1 = 0.08838834764831845f * 1.4426950408889634f;
;     __syncthreads();
;     bf16* YA = F.Y + (size_t)2 * M * 1024;
;     const unsigned* maskw = (const unsigned*)F.MASK;
;     for (int rep = 0; rep < 2; ++rep) {
;         const int j = blockIdx.x, bg = j >> 5, i = j & 31, qb = rep == 0 ? 63 - i : i, b = bg >> 1, g = bg & 1, h = 4 * g + hr;
;         const int q0 = qb * 32, tq = q0 + c; const size_t row_q = (size_t)(b * SEQ + tq);
	s_cselect_b64 s[12:13], -1, 0
	v_writelane_b32 v252, s12, 40
	s_cmp_eq_u32 s9, 14
	s_nop 0
	v_writelane_b32 v252, s13, 41
	s_cselect_b64 s[12:13], -1, 0
	v_writelane_b32 v252, s12, 42
	s_cmp_eq_u32 s9, 13
	s_nop 0
	v_writelane_b32 v252, s13, 43
	s_cselect_b64 s[12:13], -1, 0
	v_writelane_b32 v252, s12, 44
	s_cmp_eq_u32 s9, 12
	s_nop 0
	v_writelane_b32 v252, s13, 45
	s_cselect_b64 s[12:13], -1, 0
	v_writelane_b32 v252, s12, 46
	s_cmp_eq_u32 s9, 11
	s_nop 0
	v_writelane_b32 v252, s13, 47
	s_cselect_b64 s[12:13], -1, 0
	v_writelane_b32 v252, s12, 48
	s_cmp_eq_u32 s9, 10
	s_nop 0
	v_writelane_b32 v252, s13, 49
	s_cselect_b64 s[12:13], -1, 0
	v_writelane_b32 v252, s12, 50
	s_cmp_eq_u32 s9, 9
	s_nop 0
	v_writelane_b32 v252, s13, 51
	s_cselect_b64 s[12:13], -1, 0
	v_writelane_b32 v252, s12, 52
	s_cmp_eq_u32 s9, 8
	s_nop 0
	v_writelane_b32 v252, s13, 53
	s_cselect_b64 s[12:13], -1, 0
	v_writelane_b32 v252, s12, 54
	s_cmp_eq_u32 s9, 7
	s_nop 0
	v_writelane_b32 v252, s13, 55
	s_cselect_b64 s[12:13], -1, 0
	v_writelane_b32 v252, s12, 56
	s_cmp_eq_u32 s9, 6
	s_nop 0
	v_writelane_b32 v252, s13, 57
	s_cselect_b64 s[12:13], -1, 0
	v_writelane_b32 v252, s12, 58
	s_cmp_eq_u32 s9, 5
	s_nop 0
	v_writelane_b32 v252, s13, 59
	s_cselect_b64 s[12:13], -1, 0
	v_writelane_b32 v252, s12, 60
	s_cmp_eq_u32 s9, 4
	s_nop 0
	v_writelane_b32 v252, s13, 61
	s_cselect_b64 s[12:13], -1, 0
	v_writelane_b32 v252, s12, 62
	s_cmp_eq_u32 s9, 3
	s_nop 0
	v_writelane_b32 v252, s13, 63
	s_cselect_b64 s[12:13], -1, 0
	v_writelane_b32 v253, s12, 0
	s_cmp_eq_u32 s9, 2
	s_nop 0
	v_writelane_b32 v253, s13, 1
	s_cselect_b64 s[12:13], -1, 0
	v_writelane_b32 v253, s12, 2
	s_cmp_eq_u32 s9, 1
	s_nop 0
	v_writelane_b32 v253, s13, 3
	s_cselect_b64 s[12:13], -1, 0
	v_writelane_b32 v253, s12, 4
	s_cmp_eq_u32 s9, 0
	s_nop 0
	v_writelane_b32 v253, s13, 5
	s_cselect_b64 s[12:13], -1, 0
	s_lshl_b32 s1, s9, 8
	s_add_u32 s1, s4, s1
	v_writelane_b32 v253, s12, 6
	s_addc_u32 s4, s5, 0
	s_nop 0
	v_writelane_b32 v253, s13, 7
	s_add_u32 s12, s1, 0x1400
	s_addc_u32 s13, s4, 0
	v_writelane_b32 v253, s12, 8
	s_nop 1
	v_writelane_b32 v253, s13, 9
	s_add_u32 s12, s1, 0x2400
	s_addc_u32 s13, s4, 0
	v_writelane_b32 v253, s12, 10
	s_add_u32 s4, s26, 0x7400
	s_addc_u32 s5, s27, 0
	v_writelane_b32 v253, s13, 11
	v_writelane_b32 v253, s4, 12
	s_nop 1
	v_writelane_b32 v253, s5, 13
	s_add_u32 s4, s26, 0x7500
	s_addc_u32 s5, s27, 0
	v_writelane_b32 v253, s4, 14
	s_and_b32 s1, s30, 0xffffffc0
	s_lshl_b32 s88, s34, 9
	v_writelane_b32 v253, s5, 15
	v_writelane_b32 v253, s1, 16
	s_lshl_b32 s1, s8, 9
	s_add_u32 s72, s26, 0x19500000
	v_writelane_b32 v253, s1, 17
	s_addc_u32 s73, s27, 0
	s_lshl_b32 s1, s8, 5
	s_and_b32 s16, s1, 0xfffff800
	s_lshl_b32 s1, s35, 3
	s_and_b32 s1, s1, 48
	v_writelane_b32 v253, s1, 18
	s_lshl_b32 s1, s35, 8
	s_add_i32 s1, s1, 0
	s_lshr_b32 s17, s30, 8
	s_add_i32 s89, s1, 0x21800
	s_mul_i32 s1, s17, 0x4400
	s_add_i32 s4, s1, 0
	s_lshl_b32 s1, s17, 10
	v_writelane_b32 v253, s4, 19
	s_add_i32 s1, s4, s1
	s_bfe_u32 s14, s8, 0x10005
	v_writelane_b32 v253, s1, 20
	s_bfe_u32 s1, s30, 0x20006
	s_lshl_b32 s4, s14, 2
	s_or_b32 s13, s1, s4
	s_mulk_i32 s1, 0x4200
	s_add_i32 s1, s1, 0
	v_writelane_b32 v253, s1, 21
	s_mul_i32 s1, s13, 0x210
	s_add_i32 s9, s1, 0
	s_and_b32 s1, s8, 63
	v_writelane_b32 v253, s1, 22
	s_xor_b32 s1, s1, 0x7f
	v_writelane_b32 v253, s1, 23
	s_add_i32 s1, s35, 8
	v_writelane_b32 v253, s1, 24
	s_lshl_b32 s5, s1, 4
	s_lshl_b32 s1, s35, 1
	v_writelane_b32 v253, s1, 25
	s_and_b32 s1, s8, 31
	v_writelane_b32 v253, s1, 26
	s_xor_b32 s1, s1, 63
	s_add_i32 s9, s9, 0x20400
	s_lshl_b32 s4, s35, 4
	v_writelane_b32 v253, s1, 27
	s_lshl_b32 s1, s13, 7
	s_lshl_b32 s12, s17, 2
	s_add_i32 s36, s28, 0x1b0000
	s_add_u32 s18, s39, s12
	s_addc_u32 s19, s24, 0
	v_writelane_b32 v253, s18, 28
	s_add_i32 s29, s17, 2
	s_lshl_b32 s38, s17, 5
	v_writelane_b32 v253, s19, 29
	s_lshl_b32 s18, s29, 5
	v_writelane_b32 v253, s18, 30
	s_cmp_eq_u32 s17, 1
	v_writelane_b32 v253, s17, 31
	s_cselect_b64 s[18:19], -1, 0
	v_writelane_b32 v253, s18, 32
	s_cmpk_lt_u32 s30, 0x100
	s_mov_b32 s30, s15
	v_writelane_b32 v253, s19, 33
	s_cselect_b64 s[18:19], -1, 0
	s_lshl_b32 s13, s13, 8
	s_add_u32 s13, s26, s13
	v_writelane_b32 v253, s18, 34
	s_addc_u32 s15, s27, 0
	s_mul_hi_i32 s41, s16, 0x3600
	v_writelane_b32 v253, s19, 35
	s_add_u32 s18, s13, 0x1a500000
	s_addc_u32 s19, s15, 0
	v_writelane_b32 v253, s18, 36
	s_mul_i32 s13, s16, 0x3600
	s_add_u32 s15, s96, s13
	v_writelane_b32 v253, s19, 37
	v_writelane_b32 v253, s16, 38
	s_addc_u32 s16, s97, s41
	s_lshl_b32 s14, s14, 8
	s_add_u32 s18, s15, s14
	s_addc_u32 s19, s16, 0
	v_writelane_b32 v253, s18, 39
	s_cmpk_lt_i32 s31, 0x100
	s_cselect_b64 s[16:17], -1, 0
	v_writelane_b32 v253, s19, 40
	v_writelane_b32 v253, s16, 41
	s_lshl_b32 s15, s11, 5
	s_mul_hi_u32 s37, s5, 0x3600
	v_writelane_b32 v253, s17, 42
	s_add_u32 s16, s26, 0x29b00000
	v_writelane_b32 v253, s16, 43
	s_addc_u32 s16, s27, 0
	v_writelane_b32 v253, s16, 44
	s_add_u32 s16, s26, 0x10000
	v_writelane_b32 v253, s16, 45
	s_addc_u32 s16, s27, 0
	v_writelane_b32 v253, s16, 46
	s_add_u32 s16, s26, 0x29f00000
	s_addc_u32 s17, s27, 0
	v_writelane_b32 v253, s16, 47
	s_cmpk_lt_i32 s31, 0x400
	v_writelane_b32 v255, s38, 0
	v_writelane_b32 v253, s17, 48
	s_cselect_b64 s[16:17], -1, 0
	v_writelane_b32 v253, s16, 49
	s_nop 1
	v_writelane_b32 v253, s17, 50
	s_lshl_b32 s16, s11, 7
	s_cmp_lg_u64 s[22:23], 0
	s_cselect_b64 s[18:19], -1, 0
	v_readlane_b32 s22, v251, 28
	v_writelane_b32 v253, s18, 51
	s_cmpk_lt_i32 s22, 0x3f80
	s_mul_i32 s17, s11, 33
	v_writelane_b32 v253, s19, 52
	s_cselect_b64 s[18:19], -1, 0
	s_cmp_lt_i32 s11, 0
;     __host__ __device__ bool next(int i, Unit& u) const {
;         const int ti = i / subs;
;         const long L = (long)ti * G + c; if (L >= nwg) return false;
;         int wgid = (int)L; { const int q = nwg / NXCD, r = nwg % NXCD, xcd = wgid % NXCD, off = wgid / NXCD; wgid = (xcd < r ? xcd * (q + 1) : r * (q + 1) + (xcd - r) * q) + off; }
;         const int nig = WGM * nN, gid = wgid / nig, fm = gid * WGM, gsz = (nM - fm) < WGM ? (nM - fm) : WGM;
;         u.pm = fm + ((wgid % nig) % gsz); u.pn = (wgid % nig) / gsz; if (u.pn >= skip_lo) u.pn += skip_n; u.sub = i - ti * subs; return true;
;     }
	v_writelane_b32 v253, s18, 53
	s_cselect_b32 s15, s17, s15
	s_mul_i32 s17, s11, 0x81
	v_writelane_b32 v253, s19, 54
	s_cselect_b32 s18, s17, s16
	s_movk_i32 s16, 0x61
	s_cselect_b32 s16, s16, 0x60
	s_mul_i32 s16, s11, s16
	s_movk_i32 s17, 0x55
	s_cselect_b32 s17, s17, 0x54
	s_add_i32 s16, s16, s7
	s_mul_hi_i32 s19, s16, 0x2aaaaaab
	s_lshr_b32 s20, s19, 31
	s_ashr_i32 s19, s19, 5
	s_add_i32 s19, s19, s20
	s_mul_i32 s20, s19, 0xc0
	s_sub_i32 s16, s16, s20
	s_bfe_u32 s20, s16, 0x3001c
	s_mul_i32 s11, s11, s17
	s_add_i32 s20, s16, s20
	s_add_i32 s11, s11, s7
	s_and_b32 s21, s20, 0xfff8
	s_mul_hi_i32 s17, s11, 0x30c30c31
	s_sub_i32 s16, s16, s21
	s_lshr_b32 s21, s17, 31
	s_ashr_i32 s17, s17, 5
	s_add_i32 s21, s17, s21
	s_mul_i32 s17, s21, 0xa8
	s_sub_i32 s11, s11, s17
	s_lshl_b32 s17, s19, 3
	s_sext_i32_i16 s19, s20
	s_sext_i32_i16 s16, s16
	s_add_i32 s42, s17, s16
	s_ashr_i32 s16, s19, 3
	v_writelane_b32 v253, s16, 55
	s_lshr_b32 s16, s19, 3
	s_bfe_i64 s[16:17], s[16:17], 0x100000
	s_lshl_b64 s[16:17], s[16:17], 19
	v_writelane_b32 v253, s16, 56
	s_mov_b32 s20, s42
	s_ashr_i32 s43, s42, 31
	v_writelane_b32 v253, s17, 57
	s_bfe_u32 s17, s11, 0x3001c
	s_add_i32 s17, s11, s17
	s_sext_i32_i16 s19, s17
	s_and_b32 s17, s17, 0xfff8
	s_sub_i32 s17, s11, s17
	s_lshl_b32 s16, s21, 3
	s_sext_i32_i16 s17, s17
	v_writelane_b32 v253, s20, 58
	s_add_i32 s44, s16, s17
	s_ashr_i32 s16, s19, 3
	v_writelane_b32 v253, s21, 59
	s_lshl_b64 s[20:21], s[42:43], 19
	s_cmpk_lt_i32 s11, 0x80
	v_writelane_b32 v253, s20, 60
	s_cselect_b32 s11, 0, 6
	s_ashr_i32 s45, s44, 31
	v_writelane_b32 v253, s21, 61
	s_add_i32 s20, s11, s16
	s_mov_b32 s16, s44
	v_writelane_b32 v253, s16, 62
	s_ashr_i32 s21, s20, 31
	s_mul_i32 s11, s31, 3
	v_writelane_b32 v253, s17, 63
	s_lshl_b64 s[16:17], s[44:45], 20
	v_writelane_b32 v254, s16, 0
	v_readlane_b32 s23, v251, 29
	s_nop 0
	v_writelane_b32 v254, s17, 1
	s_mov_b32 s16, s20
	v_writelane_b32 v254, s16, 2
	s_nop 1
	v_writelane_b32 v254, s17, 3
	s_lshl_b64 s[16:17], s[20:21], 20
	s_cmpk_lt_i32 s31, 0xa0
	s_cselect_b32 s20, s11, s10
	s_cselect_b32 s10, 3, 2
	s_add_i32 s11, s15, s7
	s_ashr_i32 s15, s11, 31
	s_lshr_b32 s15, s15, 26
	v_writelane_b32 v254, s16, 4
	s_add_i32 s15, s11, s15
	s_add_i32 s7, s18, s7
	v_writelane_b32 v254, s17, 5
	s_and_b32 s16, s15, 0xffc0
	s_sub_i32 s11, s11, s16
	s_bfe_i32 s16, s11, 0x80000
	s_bfe_u32 s16, s16, 0x3000c
	s_add_i32 s16, s11, s16
	s_and_b32 s17, s16, 0xf8
	s_sub_i32 s11, s11, s17
	s_ashr_i32 s17, s7, 31
	s_lshr_b32 s17, s17, 24
	s_add_i32 s17, s7, s17
	s_and_b32 s18, s17, 0xff00
	s_sub_i32 s7, s7, s18
	s_sext_i32_i16 s18, s7
	v_writelane_b32 v254, s20, 6
	s_add_i32 s10, s20, s10
	s_bfe_u32 s18, s18, 0x3001c
	v_writelane_b32 v254, s10, 7
	s_ashr_i32 s10, s15, 6
	s_bfe_i32 s15, s16, 0x80000
	s_add_i32 s18, s7, s18
	s_lshl_b32 s10, s10, 3
	s_sext_i32_i16 s15, s15
	s_sext_i32_i8 s11, s11
	s_and_b32 s19, s18, 0xfff8
	s_add_i32 s20, s10, s11
	s_ashr_i32 s10, s15, 3
	s_sub_i32 s7, s7, s19
	v_writelane_b32 v254, s10, 8
	s_lshr_b32 s10, s15, 3
	s_ashr_i32 s15, s17, 8
	s_lshl_b32 s15, s15, 3
	s_sext_i32_i16 s16, s18
	s_sext_i32_i16 s7, s7
	s_add_i32 s18, s15, s7
	s_ashr_i32 s7, s16, 3
	s_lshr_b32 s16, s16, 3
	s_bfe_i64 s[16:17], s[16:17], 0x100000
	v_writelane_b32 v254, s7, 9
	s_lshl_b64 s[16:17], s[16:17], 20
	s_bfe_i64 s[10:11], s[10:11], 0x100000
	v_writelane_b32 v254, s16, 10
	s_ashr_i32 s21, s20, 31
	s_ashr_i32 s19, s18, 31
	v_writelane_b32 v254, s17, 11
	s_lshl_b64 s[16:17], s[10:11], 20
	v_writelane_b32 v254, s16, 12
	s_nop 1
	v_writelane_b32 v254, s17, 13
	s_lshl_b64 s[16:17], s[10:11], 22
	v_writelane_b32 v254, s16, 14
	s_lshl_b64 s[10:11], s[10:11], 19
	s_nop 0
	v_writelane_b32 v254, s17, 15
	v_writelane_b32 v254, s10, 16
	s_nop 1
	v_writelane_b32 v254, s11, 17
	s_lshl_b64 s[10:11], s[20:21], 20
	v_writelane_b32 v254, s10, 18
	s_nop 1
	v_writelane_b32 v254, s11, 19
	s_mov_b32 s10, s18
	v_writelane_b32 v254, s10, 20
	s_nop 1
	v_writelane_b32 v254, s11, 21
	s_lshl_b64 s[10:11], s[18:19], 20
	v_writelane_b32 v254, s10, 22
	s_nop 1
	v_writelane_b32 v254, s11, 23
	s_lshl_b64 s[10:11], s[20:21], 22
	v_writelane_b32 v254, s10, 24
	s_nop 1
	v_writelane_b32 v254, s11, 25
	s_mov_b32 s10, s20
	v_writelane_b32 v254, s10, 26
	s_nop 1
	v_writelane_b32 v254, s11, 27
;     __host__ __device__ bool next(int i, Unit& u) const {
;     ...
;         int wgid = (int)L; { const int q = nwg / NXCD, r = nwg % NXCD, xcd = wgid % NXCD, off = wgid / NXCD; wgid = (xcd < r ? xcd * (q + 1) : r * (q + 1) + (xcd - r) * q) + off; }
;         const int nig = WGM * nN, gid = wgid / nig, fm = gid * WGM, gsz = (nM - fm) < WGM ? (nM - fm) : WGM;
;         u.pm = fm + ((wgid % nig) % gsz); u.pn = (wgid % nig) / gsz; if (u.pn >= skip_lo) u.pn += skip_n; u.sub = i - ti * subs; return true;
	s_lshl_b64 s[10:11], s[20:21], 19
	v_writelane_b32 v254, s10, 28
	s_mov_b32 s20, 0xff800000
	s_nop 0
	v_writelane_b32 v254, s11, 29
	v_cmp_ge_f32_e64 s[10:11], |v2|, v0
	v_cvt_u32_f32_e32 v0, v1
	s_cmp_lg_u64 s[10:11], 0
	s_mov_b64 s[10:11], s[78:79]
	v_readfirstlane_b32 s7, v0
	s_addc_u32 s7, s7, 0
	s_mul_i32 s3, s7, s3
	s_sub_i32 s3, s6, s3
	s_add_i32 s3, s3, s2
	s_and_b32 s2, s3, 0xff
	v_writelane_b32 v254, s2, 30
	s_lshl_b32 s2, s2, 19
	s_and_b32 s3, s7, 0xff
	v_writelane_b32 v254, s2, 31
	v_writelane_b32 v254, s3, 32
	s_lshl_b32 s2, s3, 19
	v_writelane_b32 v254, s2, 33
	s_lshl_b32 s2, s29, 2
	v_writelane_b32 v254, s29, 34
	s_add_u32 s2, s39, s2
	v_writelane_b32 v254, s24, 35
	s_addc_u32 s3, s24, 0
	v_writelane_b32 v254, s2, 36
	s_mul_hi_u32 s29, s4, 0x3600
	s_mov_b32 s24, 0x10000
	v_writelane_b32 v254, s3, 37
	s_min_i32 s3, s31, 0xa0
	s_lshl_b32 s2, s31, 9
	s_lshl_b32 s6, s3, 8
	s_add_i32 s2, s2, s6
	s_lshl_b32 s6, s31, 4
	s_add_i32 s6, s35, s6
	s_lshl_b32 s3, s3, 3
	s_add_i32 s3, s6, s3
	s_lshl_b32 s6, s35, 5
	v_writelane_b32 v254, s6, 38
	s_add_i32 s2, s2, s6
	s_add_i32 s6, s3, 0xffffd800
	v_writelane_b32 v254, s6, 39
	s_add_i32 s6, s3, 0xfffff800
	v_writelane_b32 v254, s6, 40
	s_lshl_b32 s3, s3, 5
	v_writelane_b32 v254, s3, 41
	s_lshl_b32 s3, s8, 12
	v_writelane_b32 v254, s3, 42
	v_writelane_b32 v254, s2, 43
	s_add_i32 s2, s2, 0xfffb0000
	v_writelane_b32 v254, s2, 44
	s_lshl_b32 s2, s34, 12
	v_writelane_b32 v254, s2, 45
	s_mul_hi_u32 s2, s35, 0x36000
	s_add_u32 s3, s26, s28
	s_addc_u32 s2, s27, s2
	s_add_u32 s6, s3, 0xac63440
	s_addc_u32 s7, s2, 0
	s_lshl_b32 s2, s35, 6
	v_writelane_b32 v254, s6, 46
	s_and_b32 s2, s2, 0xffffff00
	s_add_i32 s2, s2, 0
	v_writelane_b32 v254, s7, 47
	v_writelane_b32 v254, s2, 48
	s_add_u32 s2, s12, 0x1f500010
	s_addc_u32 s3, 0, 0
	v_writelane_b32 v254, s2, 49
	s_or_b32 s40, s13, s14
	s_mov_b64 s[12:13], s[80:81]
	v_writelane_b32 v254, s3, 50
	v_writelane_b32 v254, s28, 51
	s_sub_i32 s2, 0, s38
	s_movk_i32 s8, 0x1000
	v_writelane_b32 v254, s29, 52
	v_writelane_b32 v254, s36, 53
	s_mov_b64 s[14:15], s[82:83]
	s_mov_b64 s[16:17], s[84:85]
	v_writelane_b32 v254, s37, 54
	v_writelane_b32 v254, s2, 55
	s_add_i32 s2, s38, 0x80
	v_writelane_b32 v254, s2, 56
	s_add_u32 s2, s40, 0xa902800
	v_writelane_b32 v254, s40, 57
	s_addc_u32 s3, s41, 0
	s_lshl_b32 s0, s0, 1
	v_writelane_b32 v254, s41, 58
	v_writelane_b32 v254, s2, 59
	s_mov_b64 s[18:19], s[86:87]
	s_mov_b64 s[28:29], 0x80
	v_writelane_b32 v254, s3, 60
	s_lshl_b32 s2, s22, 6
	s_add_i32 s2, s2, 0xfff34000
	v_writelane_b32 v254, s2, 61
	s_lshl_b32 s2, s22, 11
	s_add_i32 s2, s2, 0xfe680004
	v_writelane_b32 v254, s2, 62
	v_writelane_b32 v254, s0, 63
	s_add_i32 s0, s38, 0x90
	v_writelane_b32 v255, s0, 1
	s_lshl_b32 s0, s22, 5
	v_writelane_b32 v255, s0, 2
	s_lshl_b32 s0, s34, 8
	v_writelane_b32 v255, s0, 3
	s_lshl_b32 s0, s34, 14
	v_writelane_b32 v255, s0, 4
	s_add_i32 s0, s22, 0xe500
	v_writelane_b32 v255, s0, 5
	s_lshl_b32 s0, s34, 3
	v_writelane_b32 v255, s0, 6
	s_add_i32 s0, s22, 0xeb00
	v_writelane_b32 v255, s0, 7
	s_add_i32 s0, 0, 0x20160
	v_writelane_b32 v255, s0, 8
	s_add_i32 s0, 0, 0x20164
	v_writelane_b32 v255, s0, 9
	s_lshl_b32 s0, s1, 1
	v_writelane_b32 v255, s0, 10
	s_mov_b64 s[22:23], s[90:91]
	s_mov_b32 s6, s63
	v_writelane_b32 v255, s1, 11
	v_writelane_b32 v255, s31, 12
	v_writelane_b32 v255, s34, 13
	v_writelane_b32 v255, s8, 14
	s_nop 1
	v_writelane_b32 v255, s9, 15
	v_writelane_b32 v255, s10, 16
	v_writelane_b32 v255, s11, 17
	v_writelane_b32 v255, s12, 18
	v_writelane_b32 v255, s13, 19
	v_writelane_b32 v255, s14, 20
	v_writelane_b32 v255, s15, 21
	v_writelane_b32 v255, s16, 22
	v_writelane_b32 v255, s17, 23
	v_writelane_b32 v255, s18, 24
	v_writelane_b32 v255, s19, 25
	v_writelane_b32 v255, s20, 26
	v_writelane_b32 v255, s21, 27
	v_writelane_b32 v255, s22, 28
	v_writelane_b32 v255, s23, 29
	v_writelane_b32 v255, s35, 30
	v_writelane_b32 v255, s96, 31
	s_nop 1
	v_writelane_b32 v255, s97, 32
	v_writelane_b32 v255, s39, 33
	v_writelane_b32 v255, s76, 34
	s_nop 1
	v_writelane_b32 v255, s77, 35
	v_writelane_b32 v255, s30, 36
	v_writelane_b32 v255, s25, 37
	v_writelane_b32 v255, s88, 38
	v_writelane_b32 v255, s72, 39
	s_nop 1
	v_writelane_b32 v255, s73, 40
	v_writelane_b32 v255, s89, 41
	s_branch .LBB0_99
